# v10: + P7 side-job finish/issue moved from the SP1 load segment into the MFMA block (4-instruction chunks between MFMAs) (m1)
# speedup vs baseline: 1.0139x; 1.0037x over previous
;     __device__ __forceinline__ void finish(v4i_t& t0, v4i_t& t1, int j, int tid) const {
;         asm volatile("" : "+v"(t0), "+v"(t1));
;         const float* s0; unsigned char* d; addr(j, tid, s0, d);
;         const f32x4 r0 = __builtin_bit_cast(f32x4, t0) * 64.f, r1 = __builtin_bit_cast(f32x4, t1) * 64.f;
;         int w0 = 0, w1 = 0; w0 = __builtin_amdgcn_cvt_pk_fp8_f32(r0[0], r1[0], w0, false); w0 = __builtin_amdgcn_cvt_pk_fp8_f32(r0[1], r1[1], w0, true);
;         w1 = __builtin_amdgcn_cvt_pk_fp8_f32(r0[2], r1[2], w1, false); w1 = __builtin_amdgcn_cvt_pk_fp8_f32(r0[3], r1[3], w1, true);
;         typedef int v2is __attribute__((ext_vector_type(2))); __builtin_nontemporal_store((v2is){w0, w1}, (v2is*)d);
.Lp7vg_wd_a1:
	s_waitcnt lgkmcnt(0)
	s_barrier
	s_cmp_lt_i32 s98, 0
	s_cbranch_scc1 .Lp7vg_mmslow_a
	s_cmpk_gt_i32 s48, 0x7f
	s_cbranch_scc1 .Lp7vg_mmslow_a
	s_setprio 1
	s_waitcnt lgkmcnt(0)
	v_mfma_scale_f32_16x16x128_f8f6f4 v[202:205], v[26:33], v[58:65], v[202:205], v226, v226 op_sel_hi:[0,0,0]
	s_add_i32 s4, s98, s52
	s_add_i32 s4, s4, 1
	v_pk_mul_f32 v[70:71], v[70:71], s[14:15] op_sel_hi:[1,0]
	v_pk_mul_f32 v[72:73], v[72:73], s[14:15] op_sel_hi:[1,0]
	v_mfma_scale_f32_16x16x128_f8f6f4 v[198:201], v[18:25], v[58:65], v[198:201], v226, v226 op_sel_hi:[0,0,0]
	v_pk_mul_f32 v[74:75], v[74:75], s[14:15] op_sel_hi:[1,0]
	v_pk_mul_f32 v[76:77], v[76:77], s[14:15] op_sel_hi:[1,0]
	s_ashr_i32 s2, s4, 10
	s_ashr_i32 s3, s2, 31
	v_mfma_scale_f32_16x16x128_f8f6f4 v[186:189], v[26:33], v[50:57], v[186:189], v226, v226 op_sel_hi:[0,0,0]
	v_cvt_pk_fp8_f32 v70, v70, v74
	s_lshl_b32 s4, s4, 12
	s_lshl_b64 s[2:3], s[2:3], 22
	v_cvt_pk_fp8_f32 v70, v71, v75 op_sel:[0,0,1]
	v_mfma_scale_f32_16x16x128_f8f6f4 v[182:185], v[18:25], v[50:57], v[182:185], v226, v226 op_sel_hi:[0,0,0]
	s_and_b32 s4, s4, 0x3ff000
	v_readlane_b32 s5, v251, 50
	v_cvt_pk_fp8_f32 v71, v72, v76
	s_add_u32 s2, s5, s2
	v_mfma_scale_f32_16x16x128_f8f6f4 v[170:173], v[26:33], v[42:49], v[170:173], v226, v226 op_sel_hi:[0,0,0]
	v_readlane_b32 s5, v251, 51
	s_addc_u32 s3, s5, s3
	v_cvt_pk_fp8_f32 v71, v73, v77 op_sel:[0,0,1]
	s_add_u32 s2, s2, s4
	s_addc_u32 s3, s3, 0
	v_mfma_scale_f32_16x16x128_f8f6f4 v[166:169], v[18:25], v[42:49], v[166:169], v226, v226 op_sel_hi:[0,0,0]
	v_lshl_add_u64 v[68:69], s[2:3], 0, v[210:211]
	global_store_dwordx2 v[68:69], v[70:71], off nt
	s_add_i32 s4, s48, s53
	s_ashr_i32 s2, s4, 10
	v_mfma_scale_f32_16x16x128_f8f6f4 v[154:157], v[26:33], v[34:41], v[154:157], v226, v226 op_sel_hi:[0,0,0]
	s_ashr_i32 s3, s2, 31
	s_lshl_b64 s[2:3], s[2:3], 24
	s_lshl_b32 s4, s4, 14
	s_and_b32 s4, s4, 0xffc000
	v_mfma_scale_f32_16x16x128_f8f6f4 v[150:153], v[18:25], v[34:41], v[150:153], v226, v226 op_sel_hi:[0,0,0]
	s_setprio 0
	s_setprio 1
	s_add_u32 s2, s76, s2
	s_addc_u32 s3, s77, s3
	s_add_u32 s2, s2, s4
	s_addc_u32 s3, s3, 0
	v_mfma_scale_f32_16x16x128_f8f6f4 v[194:197], v[10:17], v[58:65], v[194:197], v226, v226 op_sel_hi:[0,0,0]
	v_lshlrev_b32_e32 v66, 2, v208
	v_lshl_add_u64 v[68:69], s[2:3], 0, v[66:67]
	v_lshl_add_u64 v[68:69], v[68:69], 0, s[16:17]
	global_load_dwordx4 v[70:73], v66, s[2:3] nt
	v_mfma_scale_f32_16x16x128_f8f6f4 v[190:193], v[2:9], v[58:65], v[190:193], v226, v226 op_sel_hi:[0,0,0]
	global_load_dwordx4 v[74:77], v[68:69], off nt
	s_mov_b32 s100, 3
	s_mov_b32 s98, s48
	s_add_i32 s48, s48, 1
	v_mfma_scale_f32_16x16x128_f8f6f4 v[178:181], v[10:17], v[50:57], v[178:181], v226, v226 op_sel_hi:[0,0,0]
	s_add_u32 s2, s42, 0xfffc0080
	s_addc_u32 s3, s43, -1
	s_cmp_eq_u32 s64, 12
	s_cselect_b32 s5, s23, s3
	s_cselect_b32 s4, s25, s2
	s_cselect_b32 s45, s35, s63
	s_cselect_b32 s44, s61, s62
	v_mfma_scale_f32_16x16x128_f8f6f4 v[174:177], v[2:9], v[50:57], v[174:177], v226, v226 op_sel_hi:[0,0,0]
	v_mfma_scale_f32_16x16x128_f8f6f4 v[162:165], v[10:17], v[42:49], v[162:165], v226, v226 op_sel_hi:[0,0,0]
	v_mfma_scale_f32_16x16x128_f8f6f4 v[158:161], v[2:9], v[42:49], v[158:161], v226, v226 op_sel_hi:[0,0,0]
	v_mfma_scale_f32_16x16x128_f8f6f4 v[146:149], v[10:17], v[34:41], v[146:149], v226, v226 op_sel_hi:[0,0,0]
	v_mfma_scale_f32_16x16x128_f8f6f4 v[142:145], v[2:9], v[34:41], v[142:145], v226, v226 op_sel_hi:[0,0,0]
	s_setprio 0
	s_branch .Lp7vg_mmjoin_a
.Lp7vg_mmslow_a:
	s_mov_b32 s100, 0
	s_cmp_lt_i32 s98, 0
	s_cbranch_scc1 .Lp7vg_nf_a
	s_add_i32 s4, s98, s52
	s_add_i32 s4, s4, 1
	v_pk_mul_f32 v[70:71], v[70:71], s[14:15] op_sel_hi:[1,0]
	v_pk_mul_f32 v[72:73], v[72:73], s[14:15] op_sel_hi:[1,0]
	v_pk_mul_f32 v[74:75], v[74:75], s[14:15] op_sel_hi:[1,0]
	v_pk_mul_f32 v[76:77], v[76:77], s[14:15] op_sel_hi:[1,0]
	s_ashr_i32 s2, s4, 10
	s_ashr_i32 s3, s2, 31
	v_cvt_pk_fp8_f32 v70, v70, v74
	s_lshl_b32 s4, s4, 12
	s_lshl_b64 s[2:3], s[2:3], 22
	v_cvt_pk_fp8_f32 v70, v71, v75 op_sel:[0,0,1]
	s_and_b32 s4, s4, 0x3ff000
	v_readlane_b32 s5, v251, 50
	v_cvt_pk_fp8_f32 v71, v72, v76
	s_add_u32 s2, s5, s2
	v_readlane_b32 s5, v251, 51
	s_addc_u32 s3, s5, s3
	v_cvt_pk_fp8_f32 v71, v73, v77 op_sel:[0,0,1]
	s_add_u32 s2, s2, s4
	s_addc_u32 s3, s3, 0
	v_lshl_add_u64 v[68:69], s[2:3], 0, v[210:211]
	global_store_dwordx2 v[68:69], v[70:71], off nt
	s_mov_b32 s100, 1

.Lp7vg_ni_a:
	s_add_u32 s2, s42, 0xfffc0080
	s_addc_u32 s3, s43, -1
	s_cmp_eq_u32 s64, 12
	s_cselect_b32 s5, s23, s3
	s_cselect_b32 s4, s25, s2
	s_cselect_b32 s45, s35, s63
	s_cselect_b32 s44, s61, s62
	s_setprio 1
	s_waitcnt lgkmcnt(0)
	v_mfma_scale_f32_16x16x128_f8f6f4 v[202:205], v[26:33], v[58:65], v[202:205], v226, v226 op_sel_hi:[0,0,0]
	v_mfma_scale_f32_16x16x128_f8f6f4 v[198:201], v[18:25], v[58:65], v[198:201], v226, v226 op_sel_hi:[0,0,0]
	v_mfma_scale_f32_16x16x128_f8f6f4 v[186:189], v[26:33], v[50:57], v[186:189], v226, v226 op_sel_hi:[0,0,0]
	v_mfma_scale_f32_16x16x128_f8f6f4 v[182:185], v[18:25], v[50:57], v[182:185], v226, v226 op_sel_hi:[0,0,0]
	v_mfma_scale_f32_16x16x128_f8f6f4 v[170:173], v[26:33], v[42:49], v[170:173], v226, v226 op_sel_hi:[0,0,0]
	v_mfma_scale_f32_16x16x128_f8f6f4 v[166:169], v[18:25], v[42:49], v[166:169], v226, v226 op_sel_hi:[0,0,0]
	v_mfma_scale_f32_16x16x128_f8f6f4 v[154:157], v[26:33], v[34:41], v[154:157], v226, v226 op_sel_hi:[0,0,0]
	v_mfma_scale_f32_16x16x128_f8f6f4 v[150:153], v[18:25], v[34:41], v[150:153], v226, v226 op_sel_hi:[0,0,0]
	s_setprio 0
	s_setprio 1
	v_mfma_scale_f32_16x16x128_f8f6f4 v[194:197], v[10:17], v[58:65], v[194:197], v226, v226 op_sel_hi:[0,0,0]
	v_mfma_scale_f32_16x16x128_f8f6f4 v[190:193], v[2:9], v[58:65], v[190:193], v226, v226 op_sel_hi:[0,0,0]
	v_mfma_scale_f32_16x16x128_f8f6f4 v[178:181], v[10:17], v[50:57], v[178:181], v226, v226 op_sel_hi:[0,0,0]
	v_mfma_scale_f32_16x16x128_f8f6f4 v[174:177], v[2:9], v[50:57], v[174:177], v226, v226 op_sel_hi:[0,0,0]
	v_mfma_scale_f32_16x16x128_f8f6f4 v[162:165], v[10:17], v[42:49], v[162:165], v226, v226 op_sel_hi:[0,0,0]
	v_mfma_scale_f32_16x16x128_f8f6f4 v[158:161], v[2:9], v[42:49], v[158:161], v226, v226 op_sel_hi:[0,0,0]
	v_mfma_scale_f32_16x16x128_f8f6f4 v[146:149], v[10:17], v[34:41], v[146:149], v226, v226 op_sel_hi:[0,0,0]
	v_mfma_scale_f32_16x16x128_f8f6f4 v[142:145], v[2:9], v[34:41], v[142:145], v226, v226 op_sel_hi:[0,0,0]
	s_setprio 0
.Lp7vg_mmjoin_a:
	s_barrier
	s_add_u32 s2, s44, 0x1000
	s_addc_u32 s3, s45, 0
	ds_read_b128 v[58:61], v236 offset:16384
	ds_read_b128 v[62:65], v236 offset:17408
	ds_read_b128 v[50:53], v236 offset:18432
	ds_read_b128 v[54:57], v236 offset:19456
	ds_read_b128 v[42:45], v236 offset:20480
	ds_read_b128 v[46:49], v236 offset:21504
	ds_read_b128 v[34:37], v236 offset:22528
	ds_read_b128 v[38:41], v236 offset:23552
	s_andn2_b64 vcc, exec, s[40:41]
	s_cmp_eq_u32 s100, 3
	s_cbranch_scc1 .Lp7dma_w5_a
	s_waitcnt vmcnt(2)
	s_branch .Lp7dma_wd_a

;     __device__ __forceinline__ void finish(v4i_t& t0, v4i_t& t1, int j, int tid) const {
;         asm volatile("" : "+v"(t0), "+v"(t1));
;         const float* s0; unsigned char* d; addr(j, tid, s0, d);
;         const f32x4 r0 = __builtin_bit_cast(f32x4, t0) * 64.f, r1 = __builtin_bit_cast(f32x4, t1) * 64.f;
;         int w0 = 0, w1 = 0; w0 = __builtin_amdgcn_cvt_pk_fp8_f32(r0[0], r1[0], w0, false); w0 = __builtin_amdgcn_cvt_pk_fp8_f32(r0[1], r1[1], w0, true);
;         w1 = __builtin_amdgcn_cvt_pk_fp8_f32(r0[2], r1[2], w1, false); w1 = __builtin_amdgcn_cvt_pk_fp8_f32(r0[3], r1[3], w1, true);
;         typedef int v2is __attribute__((ext_vector_type(2))); __builtin_nontemporal_store((v2is){w0, w1}, (v2is*)d);
.Lp7vg_wd_b1:
	s_waitcnt lgkmcnt(0)
	s_barrier
	s_cmp_lt_i32 s99, 0
	s_cbranch_scc1 .Lp7vg_mmslow_b
	s_cmpk_gt_i32 s48, 0x7f
	s_cbranch_scc1 .Lp7vg_mmslow_b
	s_setprio 1
	s_waitcnt lgkmcnt(0)
	v_mfma_scale_f32_16x16x128_f8f6f4 v[202:205], v[26:33], v[58:65], v[202:205], v226, v226 op_sel_hi:[0,0,0]
	s_add_i32 s65, s99, s52
	s_add_i32 s65, s65, 1
	v_pk_mul_f32 v[242:243], v[242:243], s[14:15] op_sel_hi:[1,0]
	v_pk_mul_f32 v[244:245], v[244:245], s[14:15] op_sel_hi:[1,0]
	v_mfma_scale_f32_16x16x128_f8f6f4 v[198:201], v[18:25], v[58:65], v[198:201], v226, v226 op_sel_hi:[0,0,0]
	v_pk_mul_f32 v[246:247], v[246:247], s[14:15] op_sel_hi:[1,0]
	v_pk_mul_f32 v[248:249], v[248:249], s[14:15] op_sel_hi:[1,0]
	s_ashr_i32 s46, s65, 10
	s_ashr_i32 s47, s46, 31
	v_mfma_scale_f32_16x16x128_f8f6f4 v[186:189], v[26:33], v[50:57], v[186:189], v226, v226 op_sel_hi:[0,0,0]
	v_cvt_pk_fp8_f32 v242, v242, v246
	s_lshl_b32 s65, s65, 12
	s_lshl_b64 s[46:47], s[46:47], 22
	v_cvt_pk_fp8_f32 v242, v243, v247 op_sel:[0,0,1]
	v_mfma_scale_f32_16x16x128_f8f6f4 v[182:185], v[18:25], v[50:57], v[182:185], v226, v226 op_sel_hi:[0,0,0]
	s_and_b32 s65, s65, 0x3ff000
	v_readlane_b32 s4, v251, 50
	v_cvt_pk_fp8_f32 v243, v244, v248
	s_add_u32 s46, s4, s46
	v_mfma_scale_f32_16x16x128_f8f6f4 v[170:173], v[26:33], v[42:49], v[170:173], v226, v226 op_sel_hi:[0,0,0]
	v_readlane_b32 s4, v251, 51
	s_addc_u32 s47, s4, s47
	v_cvt_pk_fp8_f32 v243, v245, v249 op_sel:[0,0,1]
	s_add_u32 s46, s46, s65
	s_addc_u32 s47, s47, 0
	v_mfma_scale_f32_16x16x128_f8f6f4 v[166:169], v[18:25], v[42:49], v[166:169], v226, v226 op_sel_hi:[0,0,0]
	v_lshl_add_u64 v[240:241], s[46:47], 0, v[210:211]
	global_store_dwordx2 v[240:241], v[242:243], off nt
	s_add_i32 s65, s48, s53
	s_ashr_i32 s46, s65, 10
	v_mfma_scale_f32_16x16x128_f8f6f4 v[154:157], v[26:33], v[34:41], v[154:157], v226, v226 op_sel_hi:[0,0,0]
	s_ashr_i32 s47, s46, 31
	s_lshl_b64 s[46:47], s[46:47], 24
	s_lshl_b32 s65, s65, 14
	s_and_b32 s65, s65, 0xffc000
	v_mfma_scale_f32_16x16x128_f8f6f4 v[150:153], v[18:25], v[34:41], v[150:153], v226, v226 op_sel_hi:[0,0,0]
	s_setprio 0
	s_setprio 1
	s_add_u32 s46, s76, s46
	s_addc_u32 s47, s77, s47
	s_add_u32 s46, s46, s65
	s_addc_u32 s47, s47, 0
	v_mfma_scale_f32_16x16x128_f8f6f4 v[194:197], v[10:17], v[58:65], v[194:197], v226, v226 op_sel_hi:[0,0,0]
	v_lshlrev_b32_e32 v66, 2, v208
	v_lshl_add_u64 v[240:241], s[46:47], 0, v[66:67]
	v_lshl_add_u64 v[240:241], v[240:241], 0, s[16:17]
	global_load_dwordx4 v[242:245], v66, s[46:47] nt
	v_mfma_scale_f32_16x16x128_f8f6f4 v[190:193], v[2:9], v[58:65], v[190:193], v226, v226 op_sel_hi:[0,0,0]
	global_load_dwordx4 v[246:249], v[240:241], off nt
	s_mov_b32 s100, 3
	s_mov_b32 s99, s48
	s_add_i32 s48, s48, 1
	v_mfma_scale_f32_16x16x128_f8f6f4 v[178:181], v[10:17], v[50:57], v[178:181], v226, v226 op_sel_hi:[0,0,0]
	s_add_u32 s46, s44, 0x84000
	s_addc_u32 s47, s45, 0
	v_mfma_scale_f32_16x16x128_f8f6f4 v[174:177], v[2:9], v[50:57], v[174:177], v226, v226 op_sel_hi:[0,0,0]
	v_mfma_scale_f32_16x16x128_f8f6f4 v[162:165], v[10:17], v[42:49], v[162:165], v226, v226 op_sel_hi:[0,0,0]
	v_mfma_scale_f32_16x16x128_f8f6f4 v[158:161], v[2:9], v[42:49], v[158:161], v226, v226 op_sel_hi:[0,0,0]
	v_mfma_scale_f32_16x16x128_f8f6f4 v[146:149], v[10:17], v[34:41], v[146:149], v226, v226 op_sel_hi:[0,0,0]
	v_mfma_scale_f32_16x16x128_f8f6f4 v[142:145], v[2:9], v[34:41], v[142:145], v226, v226 op_sel_hi:[0,0,0]
	s_setprio 0
	s_branch .Lp7vg_mmjoin_b
.Lp7vg_mmslow_b:
	s_mov_b32 s100, 0
	s_cmp_lt_i32 s99, 0
	s_cbranch_scc1 .Lp7vg_nf_b
	s_add_i32 s65, s99, s52
	s_add_i32 s65, s65, 1
	v_pk_mul_f32 v[242:243], v[242:243], s[14:15] op_sel_hi:[1,0]
	v_pk_mul_f32 v[244:245], v[244:245], s[14:15] op_sel_hi:[1,0]
	v_pk_mul_f32 v[246:247], v[246:247], s[14:15] op_sel_hi:[1,0]
	v_pk_mul_f32 v[248:249], v[248:249], s[14:15] op_sel_hi:[1,0]
	s_ashr_i32 s46, s65, 10
	s_ashr_i32 s47, s46, 31
	v_cvt_pk_fp8_f32 v242, v242, v246
	s_lshl_b32 s65, s65, 12
	s_lshl_b64 s[46:47], s[46:47], 22
	v_cvt_pk_fp8_f32 v242, v243, v247 op_sel:[0,0,1]
	s_and_b32 s65, s65, 0x3ff000
	v_readlane_b32 s4, v251, 50
	v_cvt_pk_fp8_f32 v243, v244, v248
	s_add_u32 s46, s4, s46
	v_readlane_b32 s4, v251, 51
	s_addc_u32 s47, s4, s47
	v_cvt_pk_fp8_f32 v243, v245, v249 op_sel:[0,0,1]
	s_add_u32 s46, s46, s65
	s_addc_u32 s47, s47, 0
	v_lshl_add_u64 v[240:241], s[46:47], 0, v[210:211]
	global_store_dwordx2 v[240:241], v[242:243], off nt
	s_mov_b32 s100, 1

.Lp7vg_ni_b:
	s_add_u32 s46, s44, 0x84000
	s_addc_u32 s47, s45, 0
	s_setprio 1
	s_waitcnt lgkmcnt(0)
	v_mfma_scale_f32_16x16x128_f8f6f4 v[202:205], v[26:33], v[58:65], v[202:205], v226, v226 op_sel_hi:[0,0,0]
	v_mfma_scale_f32_16x16x128_f8f6f4 v[198:201], v[18:25], v[58:65], v[198:201], v226, v226 op_sel_hi:[0,0,0]
	v_mfma_scale_f32_16x16x128_f8f6f4 v[186:189], v[26:33], v[50:57], v[186:189], v226, v226 op_sel_hi:[0,0,0]
	v_mfma_scale_f32_16x16x128_f8f6f4 v[182:185], v[18:25], v[50:57], v[182:185], v226, v226 op_sel_hi:[0,0,0]
	v_mfma_scale_f32_16x16x128_f8f6f4 v[170:173], v[26:33], v[42:49], v[170:173], v226, v226 op_sel_hi:[0,0,0]
	v_mfma_scale_f32_16x16x128_f8f6f4 v[166:169], v[18:25], v[42:49], v[166:169], v226, v226 op_sel_hi:[0,0,0]
	v_mfma_scale_f32_16x16x128_f8f6f4 v[154:157], v[26:33], v[34:41], v[154:157], v226, v226 op_sel_hi:[0,0,0]
	v_mfma_scale_f32_16x16x128_f8f6f4 v[150:153], v[18:25], v[34:41], v[150:153], v226, v226 op_sel_hi:[0,0,0]
	s_setprio 0
	s_setprio 1
	v_mfma_scale_f32_16x16x128_f8f6f4 v[194:197], v[10:17], v[58:65], v[194:197], v226, v226 op_sel_hi:[0,0,0]
	v_mfma_scale_f32_16x16x128_f8f6f4 v[190:193], v[2:9], v[58:65], v[190:193], v226, v226 op_sel_hi:[0,0,0]
	v_mfma_scale_f32_16x16x128_f8f6f4 v[178:181], v[10:17], v[50:57], v[178:181], v226, v226 op_sel_hi:[0,0,0]
	v_mfma_scale_f32_16x16x128_f8f6f4 v[174:177], v[2:9], v[50:57], v[174:177], v226, v226 op_sel_hi:[0,0,0]
	v_mfma_scale_f32_16x16x128_f8f6f4 v[162:165], v[10:17], v[42:49], v[162:165], v226, v226 op_sel_hi:[0,0,0]
	v_mfma_scale_f32_16x16x128_f8f6f4 v[158:161], v[2:9], v[42:49], v[158:161], v226, v226 op_sel_hi:[0,0,0]
	v_mfma_scale_f32_16x16x128_f8f6f4 v[146:149], v[10:17], v[34:41], v[146:149], v226, v226 op_sel_hi:[0,0,0]
	v_mfma_scale_f32_16x16x128_f8f6f4 v[142:145], v[2:9], v[34:41], v[142:145], v226, v226 op_sel_hi:[0,0,0]
	s_setprio 0
.Lp7vg_mmjoin_b:
	s_barrier
	ds_read_b128 v[58:61], v236 offset:49152
	ds_read_b128 v[62:65], v236 offset:50176
	ds_read_b128 v[50:53], v236 offset:51200
	ds_read_b128 v[54:57], v236 offset:52224
	ds_read_b128 v[42:45], v236 offset:53248
	ds_read_b128 v[46:49], v236 offset:54272
	ds_read_b128 v[34:37], v236 offset:55296
	ds_read_b128 v[38:41], v236 offset:56320
	s_and_b64 vcc, exec, s[2:3]
	s_cmp_eq_u32 s100, 3
	s_cbranch_scc1 .Lp7dma_w5_b
	s_waitcnt vmcnt(2)
	s_branch .Lp7dma_wd_b
